# DIFF loop head: second QK MFMA issued before the second K/V DMA (DMA address temp moved out of the score registers)
# baseline (speedup 1.0000x reference)
.LBB0_953:
	v_mfma_f32_32x32x16_bf16 v[114:129], v[98:101], v[130:133], 0
	s_min_i32 s28, s26, 0x101
	s_lshl_b32 s28, s28, 13
	s_add_i32 s88, s28, 0x4000
	s_lshl_b32 s28, s22, 14
	s_add_i32 s28, s21, s28
	v_lshl_add_u64 v[236:237], v[174:175], 0, s[88:89]
	s_mov_b32 m0, s28
	v_lshl_add_u32 v181, s27, 14, v0
	global_load_lds_dwordx4 v[236:237], off
	v_mfma_f32_32x32x16_bf16 v[98:113], v[102:105], v[134:137], 0
	v_lshl_add_u64 v[236:237], v[176:177], 0, s[88:89]
	s_add_i32 m0, s28, 0x2000
	s_lshl_b32 s28, s25, 14
	global_load_lds_dwordx4 v[236:237], off
	ds_read_b128 v[190:193], v181 offset:12288
	v_add_u32_e32 v189, s28, v0
	v_lshl_add_u32 v210, s23, 14, v188
	v_exp_f32_e32 v194, v82
	v_exp_f32_e32 v196, v83
	v_exp_f32_e32 v198, v84
	v_exp_f32_e32 v200, v85
	ds_read_b128 v[82:85], v181 offset:12800
	v_cvt_pk_bf16_f32 v170, v194, v196
	v_add_f32_e32 v232, v194, v232
	v_add_f32_e32 v232, v196, v232
	v_cvt_pk_bf16_f32 v171, v198, v200
	v_add_f32_e32 v232, v198, v232
	v_add_f32_e32 v232, v200, v232
	v_exp_f32_e32 v202, v86
	v_exp_f32_e32 v204, v87
	s_waitcnt lgkmcnt(3)
	v_mfma_f32_32x32x16_bf16 v[114:129], v[162:165], v[138:141], v[114:129]
	v_cvt_pk_bf16_f32 v172, v202, v204
	v_add_f32_e32 v232, v202, v232
	v_add_f32_e32 v232, v204, v232
	v_exp_f32_e32 v206, v88
	v_exp_f32_e32 v208, v89
	s_waitcnt lgkmcnt(2)
	v_mfma_f32_32x32x16_bf16 v[98:113], v[166:169], v[142:145], v[98:113]
	v_exp_f32_e32 v168, v92
	v_exp_f32_e32 v166, v93
	v_cvt_pk_bf16_f32 v173, v206, v208
	v_add_f32_e32 v232, v206, v232
	v_add_f32_e32 v232, v208, v232
	v_exp_f32_e32 v214, v90
	v_exp_f32_e32 v216, v91
	s_waitcnt lgkmcnt(1)
	v_mfma_f32_32x32x16_bf16 v[34:49], v[190:193], v[150:153], v[34:49]
	ds_read_b128 v[86:89], v181 offset:14336
	v_cvt_pk_bf16_f32 v162, v214, v216
	v_add_f32_e32 v232, v214, v232
	v_add_f32_e32 v232, v216, v232
	v_cvt_pk_bf16_f32 v163, v168, v166
	v_add_f32_e32 v232, v168, v232
	v_add_f32_e32 v232, v166, v232
	v_exp_f32_e32 v182, v94
	v_exp_f32_e32 v180, v95
	s_waitcnt lgkmcnt(1)
	v_mfma_f32_32x32x16_bf16 v[50:65], v[82:85], v[150:153], v[50:65]
	ds_read_b128 v[90:93], v181 offset:14848
	v_cvt_pk_bf16_f32 v164, v182, v180
	v_add_f32_e32 v232, v182, v232
	v_add_f32_e32 v232, v180, v232
	v_exp_f32_e32 v186, v96
	v_exp_f32_e32 v184, v97
	v_mfma_f32_32x32x16_bf16 v[2:17], v[190:193], v[158:161], v[2:17]
	v_cvt_pk_bf16_f32 v165, v186, v184
	v_add_f32_e32 v232, v186, v232
	v_add_f32_e32 v232, v184, v232
	v_exp_f32_e32 v195, v66
	v_exp_f32_e32 v197, v67
	v_exp_f32_e32 v199, v68
	v_exp_f32_e32 v201, v69
	v_mfma_f32_32x32x16_bf16 v[18:33], v[82:85], v[158:161], v[18:33]
	v_cvt_pk_bf16_f32 v158, v195, v197
	v_add_f32_e32 v233, v195, v233
	v_add_f32_e32 v233, v197, v233
	v_cvt_pk_bf16_f32 v159, v199, v201
	v_add_f32_e32 v233, v199, v233
	v_add_f32_e32 v233, v201, v233
	v_exp_f32_e32 v203, v70
	v_exp_f32_e32 v205, v71
	s_waitcnt lgkmcnt(1)
	v_mfma_f32_32x32x16_bf16 v[34:49], v[86:89], v[154:157], v[34:49]
	ds_read_b128 v[66:69], v210
	v_cvt_pk_bf16_f32 v160, v203, v205
	v_add_f32_e32 v233, v203, v233
	v_add_f32_e32 v233, v205, v233
	v_exp_f32_e32 v207, v72
	v_exp_f32_e32 v209, v73
	s_waitcnt lgkmcnt(1)
	v_mfma_f32_32x32x16_bf16 v[50:65], v[90:93], v[154:157], v[50:65]
	ds_read_b128 v[70:73], v210 offset:4096
	v_exp_f32_e32 v169, v76
	v_exp_f32_e32 v167, v77
	v_cvt_pk_bf16_f32 v161, v207, v209
	v_add_f32_e32 v233, v207, v233
	v_add_f32_e32 v233, v209, v233
	v_exp_f32_e32 v215, v74
	v_exp_f32_e32 v217, v75
	v_mfma_f32_32x32x16_bf16 v[2:17], v[86:89], v[146:149], v[2:17]
	ds_read_b128 v[152:155], v210 offset:2048
	v_cvt_pk_bf16_f32 v190, v215, v217
	v_add_f32_e32 v233, v215, v233
	v_add_f32_e32 v233, v217, v233
	v_cvt_pk_bf16_f32 v191, v169, v167
	v_add_f32_e32 v233, v169, v233
	v_add_f32_e32 v233, v167, v233
	v_exp_f32_e32 v183, v78
	v_exp_f32_e32 v181, v79
	v_mfma_f32_32x32x16_bf16 v[18:33], v[90:93], v[146:149], v[18:33]
	v_exp_f32_e32 v187, v80
	v_exp_f32_e32 v185, v81
	ds_read_b128 v[194:197], v210 offset:6144
	v_cvt_pk_bf16_f32 v192, v183, v181
	v_add_f32_e32 v233, v183, v233
	v_add_f32_e32 v233, v181, v233
	v_cvt_pk_bf16_f32 v193, v187, v185
	v_add_f32_e32 v233, v187, v233
	v_add_f32_e32 v233, v185, v233
	s_waitcnt lgkmcnt(3)
	v_mfma_f32_32x32x16_bf16 v[82:97], v[66:69], v[130:133], 0
	ds_read_b128 v[146:149], v189 offset:8192
	v_exp_f32_e32 v198, v114
	v_exp_f32_e32 v200, v115
	v_exp_f32_e32 v202, v116
	v_exp_f32_e32 v204, v117
	s_waitcnt lgkmcnt(3)
	v_mfma_f32_32x32x16_bf16 v[66:81], v[70:73], v[134:137], 0
	ds_read_b128 v[114:117], v189 offset:8704
	v_cvt_pk_bf16_f32 v150, v198, v200
	v_add_f32_e32 v232, v198, v232
	v_add_f32_e32 v232, v200, v232
	v_cvt_pk_bf16_f32 v151, v202, v204
	v_add_f32_e32 v232, v202, v232
	v_add_f32_e32 v232, v204, v232
	v_exp_f32_e32 v206, v118
	v_exp_f32_e32 v208, v119
	s_waitcnt lgkmcnt(3)
	v_mfma_f32_32x32x16_bf16 v[82:97], v[152:155], v[138:141], v[82:97]
	v_cvt_pk_bf16_f32 v152, v206, v208
	v_add_f32_e32 v232, v206, v232
	v_add_f32_e32 v232, v208, v232
	v_exp_f32_e32 v214, v120
	v_exp_f32_e32 v216, v121
	s_waitcnt lgkmcnt(2)
	v_mfma_f32_32x32x16_bf16 v[66:81], v[194:197], v[142:145], v[66:81]
	v_cvt_pk_bf16_f32 v153, v214, v216
	v_add_f32_e32 v232, v214, v232
	v_add_f32_e32 v232, v216, v232
	v_exp_f32_e32 v194, v122
	v_exp_f32_e32 v196, v123
	v_exp_f32_e32 v218, v124
	v_exp_f32_e32 v220, v125
	s_waitcnt lgkmcnt(1)
	v_mfma_f32_32x32x16_bf16 v[34:49], v[146:149], v[170:173], v[34:49]
	ds_read_b128 v[118:121], v189 offset:10240
	v_cvt_pk_bf16_f32 v154, v194, v196
	v_add_f32_e32 v232, v194, v232
	v_add_f32_e32 v232, v196, v232
	v_cvt_pk_bf16_f32 v155, v218, v220
	v_add_f32_e32 v232, v218, v232
	v_add_f32_e32 v232, v220, v232
	v_exp_f32_e32 v126, v126
	v_exp_f32_e32 v222, v127
	s_waitcnt lgkmcnt(1)
	v_mfma_f32_32x32x16_bf16 v[50:65], v[114:117], v[170:173], v[50:65]
	ds_read_b128 v[122:125], v189 offset:10752
	v_cvt_pk_bf16_f32 v156, v126, v222
	v_add_f32_e32 v232, v126, v232
	v_add_f32_e32 v232, v222, v232
	v_exp_f32_e32 v128, v128
	v_exp_f32_e32 v170, v129
	v_mfma_f32_32x32x16_bf16 v[2:17], v[146:149], v[158:161], v[2:17]
	v_cvt_pk_bf16_f32 v157, v128, v170
	v_add_f32_e32 v232, v128, v232
	v_add_f32_e32 v232, v170, v232
	v_exp_f32_e32 v199, v98
	v_exp_f32_e32 v201, v99
	v_exp_f32_e32 v203, v100
	v_exp_f32_e32 v205, v101
	v_mfma_f32_32x32x16_bf16 v[18:33], v[114:117], v[158:161], v[18:33]
	v_cvt_pk_bf16_f32 v158, v199, v201
	v_add_f32_e32 v233, v199, v233
	v_add_f32_e32 v233, v201, v233
	v_cvt_pk_bf16_f32 v159, v203, v205
	v_add_f32_e32 v233, v203, v233
	v_add_f32_e32 v233, v205, v233
	v_exp_f32_e32 v207, v102
	v_exp_f32_e32 v209, v103
	s_waitcnt lgkmcnt(1)
	v_mfma_f32_32x32x16_bf16 v[34:49], v[118:121], v[162:165], v[34:49]
	ds_read_b128 v[98:101], v210 offset:512
	v_cvt_pk_bf16_f32 v160, v207, v209
	v_add_f32_e32 v233, v207, v233
	v_add_f32_e32 v233, v209, v233
	v_exp_f32_e32 v215, v104
	v_exp_f32_e32 v217, v105
	s_waitcnt lgkmcnt(1)
	v_mfma_f32_32x32x16_bf16 v[50:65], v[122:125], v[162:165], v[50:65]
	ds_read_b128 v[102:105], v210 offset:4608
	v_cvt_pk_bf16_f32 v161, v215, v217
	v_add_f32_e32 v233, v215, v233
	v_add_f32_e32 v233, v217, v233
	v_exp_f32_e32 v195, v106
	v_exp_f32_e32 v197, v107
	v_exp_f32_e32 v219, v108
	v_exp_f32_e32 v221, v109
	v_mfma_f32_32x32x16_bf16 v[2:17], v[118:121], v[190:193], v[2:17]
	ds_read_b128 v[162:165], v210 offset:2560
	v_cvt_pk_bf16_f32 v146, v195, v197
	v_add_f32_e32 v233, v195, v233
	v_add_f32_e32 v233, v197, v233
	v_cvt_pk_bf16_f32 v147, v219, v221
	v_add_f32_e32 v233, v219, v233
	v_add_f32_e32 v233, v221, v233
	v_exp_f32_e32 v127, v110
	v_exp_f32_e32 v223, v111
	v_mfma_f32_32x32x16_bf16 v[18:33], v[122:125], v[190:193], v[18:33]
	v_exp_f32_e32 v129, v112
	ds_read_b128 v[166:169], v210 offset:6656
	v_exp_f32_e32 v171, v113
	v_cvt_pk_bf16_f32 v148, v127, v223
	v_add_f32_e32 v233, v127, v233
	v_add_f32_e32 v233, v223, v233
	v_cvt_pk_bf16_f32 v149, v129, v171
	v_add_f32_e32 v233, v129, v233
	v_add_f32_e32 v233, v171, v233
	s_add_i32 s27, s22, 1
	s_waitcnt vmcnt(0)
	s_and_b32 s28, s27, 3
	s_add_i32 s26, s26, 1
	s_cmpk_eq_i32 s26, 0x104
	s_mov_b32 s27, s25
	s_mov_b32 s25, s23
	s_mov_b32 s23, s22
	s_mov_b32 s22, s28
	s_waitcnt vmcnt(0) lgkmcnt(0)
	s_barrier
	s_cbranch_scc0 .LBB0_953
	v_mov_b32_e32 v178, v232
	v_mov_b32_e32 v179, v233
	ds_read_b128 v[66:69], v189 offset:12288
	ds_read_b128 v[70:73], v189 offset:12800
	v_mov_b32_e32 v0, v230
	s_waitcnt lgkmcnt(1)
	v_mfma_f32_32x32x16_bf16 v[34:49], v[66:69], v[150:153], v[34:49]
	s_waitcnt lgkmcnt(0)
	v_mfma_f32_32x32x16_bf16 v[50:65], v[70:73], v[150:153], v[50:65]
	v_mfma_f32_32x32x16_bf16 v[2:17], v[66:69], v[158:161], v[2:17]
	v_mfma_f32_32x32x16_bf16 v[18:33], v[70:73], v[158:161], v[18:33]
	ds_read_b128 v[68:71], v189 offset:14336
	ds_read_b128 v[72:75], v189 offset:14848
	v_mbcnt_lo_u32_b32 v76, -1, 0
	v_mbcnt_hi_u32_b32 v76, -1, v76
	v_mbcnt_lo_u32_b32 v77, -1, 0
	v_mbcnt_hi_u32_b32 v77, -1, v77
	global_load_dwordx2 v[66:67], v1, s[6:7]
	v_lshlrev_b32_e32 v77, 2, v77
	v_xor_b32_e32 v77, 0x80, v77
	v_lshlrev_b32_e32 v76, 2, v76
	ds_bpermute_b32 v77, v77, v179
	v_xor_b32_e32 v76, 0x80, v76
	ds_bpermute_b32 v76, v76, v178
	s_waitcnt lgkmcnt(3)
	v_mfma_f32_32x32x16_bf16 v[2:17], v[68:71], v[146:149], v[2:17]
	v_readfirstlane_b32 s21, v0
	s_ashr_i32 s21, s21, 1
	s_andn2_b32 s21, s21, 31
	s_cmpk_lt_i32 s21, 0x100
	s_waitcnt lgkmcnt(2)
	v_mfma_f32_32x32x16_bf16 v[18:33], v[72:75], v[146:149], v[18:33]
	v_mfma_f32_32x32x16_bf16 v[34:49], v[68:71], v[154:157], v[34:49]
	s_waitcnt lgkmcnt(1)
	v_add_f32_e32 v70, v179, v77
	v_mbcnt_lo_u32_b32 v68, -1, 0
	v_mbcnt_hi_u32_b32 v68, -1, v68
	v_rcp_f32_e32 v70, v70
	v_lshlrev_b32_e32 v69, 2, v68
	s_waitcnt lgkmcnt(0)
	v_add_f32_e32 v68, v178, v76
	v_rcp_f32_e32 v68, v68
	s_waitcnt vmcnt(0)
	v_mul_f32_e32 v66, v66, v70
	v_mfma_f32_32x32x16_bf16 v[50:65], v[72:75], v[154:157], v[50:65]
	v_mul_f32_e64 v2, v2, v66
	v_mul_f32_e64 v3, v3, v66
	v_mul_f32_e64 v18, v18, v66
	v_mul_f32_e64 v19, v19, v66
	v_mul_f32_e64 v4, v4, v66
	v_mul_f32_e64 v5, v5, v66
	v_pk_mul_f32 v[20:21], v[20:21], v[66:67] op_sel_hi:[1,0]
	v_pk_mul_f32 v[70:71], v[24:25], v[66:67] op_sel_hi:[1,0]
	v_pk_fma_f32 v[24:25], v[34:35], v[68:69], v[2:3] op_sel_hi:[1,0,1] neg_lo:[0,0,1] neg_hi:[0,0,1]
	v_pk_mul_f32 v[72:73], v[26:27], v[66:67] op_sel_hi:[1,0]
	s_nop 1
	v_pk_fma_f32 v[2:3], v[50:51], v[68:69], v[18:19] op_sel_hi:[1,0,1] neg_lo:[0,0,1] neg_hi:[0,0,1]
	v_pk_fma_f32 v[26:27], v[36:37], v[68:69], v[4:5] op_sel_hi:[1,0,1] neg_lo:[0,0,1] neg_hi:[0,0,1]
	v_pk_fma_f32 v[4:5], v[52:53], v[68:69], v[20:21] op_sel_hi:[1,0,1] neg_lo:[0,0,1] neg_hi:[0,0,1]
	v_pk_mul_f32 v[18:19], v[2:3], v[2:3]
	v_pk_mul_f32 v[6:7], v[6:7], v[66:67] op_sel_hi:[1,0]
	v_pk_mul_f32 v[22:23], v[22:23], v[66:67] op_sel_hi:[1,0]
	v_pk_mul_f32 v[36:37], v[4:5], v[4:5]
	v_pk_fma_f32 v[18:19], v[24:25], v[24:25], v[18:19]
	v_pk_mul_f32 v[74:75], v[28:29], v[66:67] op_sel_hi:[1,0]
	v_pk_fma_f32 v[28:29], v[38:39], v[68:69], v[6:7] op_sel_hi:[1,0,1] neg_lo:[0,0,1] neg_hi:[0,0,1]
	v_pk_fma_f32 v[6:7], v[54:55], v[68:69], v[22:23] op_sel_hi:[1,0,1] neg_lo:[0,0,1] neg_hi:[0,0,1]
	v_pk_fma_f32 v[36:37], v[26:27], v[26:27], v[36:37]
	v_add_f32_e32 v18, v18, v19
	v_pk_mul_f32 v[8:9], v[8:9], v[66:67] op_sel_hi:[1,0]
	v_pk_mul_f32 v[38:39], v[6:7], v[6:7]
	v_add_f32_e32 v18, v36, v18
	v_pk_mul_f32 v[76:77], v[30:31], v[66:67] op_sel_hi:[1,0]
	v_pk_fma_f32 v[30:31], v[40:41], v[68:69], v[8:9] op_sel_hi:[1,0,1] neg_lo:[0,0,1] neg_hi:[0,0,1]
	v_pk_fma_f32 v[8:9], v[56:57], v[68:69], v[70:71] op_sel_hi:[1,0,1] neg_lo:[0,0,1] neg_hi:[0,0,1]
	v_pk_fma_f32 v[38:39], v[28:29], v[28:29], v[38:39]
	v_add_f32_e32 v18, v37, v18
	v_pk_mul_f32 v[10:11], v[10:11], v[66:67] op_sel_hi:[1,0]
	v_pk_mul_f32 v[40:41], v[8:9], v[8:9]
	v_add_f32_e32 v18, v38, v18
	v_pk_mul_f32 v[78:79], v[32:33], v[66:67] op_sel_hi:[1,0]
	v_pk_fma_f32 v[32:33], v[42:43], v[68:69], v[10:11] op_sel_hi:[1,0,1] neg_lo:[0,0,1] neg_hi:[0,0,1]
	v_pk_fma_f32 v[10:11], v[58:59], v[68:69], v[72:73] op_sel_hi:[1,0,1] neg_lo:[0,0,1] neg_hi:[0,0,1]
	v_pk_fma_f32 v[40:41], v[30:31], v[30:31], v[40:41]
	v_add_f32_e32 v18, v39, v18
	v_pk_mul_f32 v[12:13], v[12:13], v[66:67] op_sel_hi:[1,0]
	v_pk_mul_f32 v[42:43], v[10:11], v[10:11]
	v_add_f32_e32 v18, v40, v18
	v_pk_fma_f32 v[34:35], v[44:45], v[68:69], v[12:13] op_sel_hi:[1,0,1] neg_lo:[0,0,1] neg_hi:[0,0,1]
	v_pk_fma_f32 v[12:13], v[60:61], v[68:69], v[74:75] op_sel_hi:[1,0,1] neg_lo:[0,0,1] neg_hi:[0,0,1]
	v_pk_fma_f32 v[42:43], v[32:33], v[32:33], v[42:43]
	v_add_f32_e32 v18, v41, v18
	v_pk_mul_f32 v[14:15], v[14:15], v[66:67] op_sel_hi:[1,0]
	v_pk_mul_f32 v[44:45], v[12:13], v[12:13]
	v_add_f32_e32 v18, v42, v18
	v_pk_fma_f32 v[20:21], v[46:47], v[68:69], v[14:15] op_sel_hi:[1,0,1] neg_lo:[0,0,1] neg_hi:[0,0,1]
	v_pk_fma_f32 v[14:15], v[62:63], v[68:69], v[76:77] op_sel_hi:[1,0,1] neg_lo:[0,0,1] neg_hi:[0,0,1]
	v_pk_fma_f32 v[44:45], v[34:35], v[34:35], v[44:45]
	v_add_f32_e32 v18, v43, v18
	v_pk_mul_f32 v[16:17], v[16:17], v[66:67] op_sel_hi:[1,0]
	v_pk_mul_f32 v[46:47], v[14:15], v[14:15]
	v_add_f32_e32 v18, v44, v18
	v_pk_fma_f32 v[22:23], v[48:49], v[68:69], v[16:17] op_sel_hi:[1,0,1] neg_lo:[0,0,1] neg_hi:[0,0,1]
	v_pk_fma_f32 v[16:17], v[64:65], v[68:69], v[78:79] op_sel_hi:[1,0,1] neg_lo:[0,0,1] neg_hi:[0,0,1]
	v_pk_fma_f32 v[46:47], v[20:21], v[20:21], v[46:47]
	v_add_f32_e32 v18, v45, v18
	v_pk_mul_f32 v[48:49], v[16:17], v[16:17]
	v_add_f32_e32 v18, v46, v18
	v_pk_fma_f32 v[48:49], v[22:23], v[22:23], v[48:49]
	v_add_f32_e32 v18, v47, v18
	v_add_f32_e32 v18, v48, v18
	v_add_f32_e32 v36, v49, v18
	v_xor_b32_e32 v18, 0x80, v69
	ds_bpermute_b32 v37, v18, v36
	s_cbranch_scc0 .LBB0_951
	s_waitcnt lgkmcnt(0)
	v_add_f32_e32 v36, v36, v37
	v_fmamk_f32 v36, v36, 0x3c800000, v224
	v_cmp_gt_f32_e32 vcc, s31, v36
	v_mul_f32_e32 v37, 0x4b800000, v36
	v_and_or_b32 v18, v0, 31, s21
	v_cndmask_b32_e32 v36, v36, v37, vcc
	v_rsq_f32_e32 v36, v36
	v_lshrrev_b32_e32 v0, 3, v0
	v_and_b32_e32 v0, 4, v0
	v_lshlrev_b32_e32 v41, 2, v0
	v_mul_f32_e32 v37, 0x45800000, v36
	v_cndmask_b32_e32 v36, v36, v37, vcc
	v_mul_f32_e32 v40, v67, v36
	global_load_dwordx4 v[36:39], v41, s[8:9] offset:128
	s_lshl_b64 s[10:11], s[10:11], 11
	s_add_u32 s10, s2, s10
	s_addc_u32 s11, s3, s11
	s_lshl_b32 s20, s20, 1
	s_add_u32 s10, s10, s20
	v_ashrrev_i32_e32 v19, 31, v18
	s_addc_u32 s11, s11, 0
	v_lshlrev_b64 v[18:19], 11, v[18:19]
	v_lshl_add_u64 v[18:19], s[10:11], 0, v[18:19]
	v_lshlrev_b32_e32 v0, 1, v0
	v_lshl_add_u64 v[18:19], v[18:19], 0, v[0:1]
	s_waitcnt vmcnt(0)
	v_pk_mul_f32 v[36:37], v[40:41], v[36:37] op_sel_hi:[0,1]
	v_pk_mul_f32 v[2:3], v[2:3], v[36:37]
	v_pk_mul_f32 v[36:37], v[40:41], v[38:39] op_sel_hi:[0,1]
	v_pk_mul_f32 v[4:5], v[4:5], v[36:37]
	global_load_dwordx4 v[36:39], v41, s[8:9] offset:160
	v_cvt_pk_bf16_f32 v2, v2, v3
	v_cvt_pk_bf16_f32 v3, v4, v5
	s_waitcnt vmcnt(0)
	v_pk_mul_f32 v[36:37], v[40:41], v[36:37] op_sel_hi:[0,1]
	v_pk_mul_f32 v[6:7], v[6:7], v[36:37]
	v_pk_mul_f32 v[36:37], v[40:41], v[38:39] op_sel_hi:[0,1]
	v_pk_mul_f32 v[8:9], v[8:9], v[36:37]
	global_load_dwordx4 v[36:39], v41, s[8:9] offset:192
	v_cvt_pk_bf16_f32 v4, v6, v7
	v_cvt_pk_bf16_f32 v5, v8, v9
	s_waitcnt vmcnt(0)
	v_pk_mul_f32 v[36:37], v[40:41], v[36:37] op_sel_hi:[0,1]
	v_pk_mul_f32 v[10:11], v[10:11], v[36:37]
	v_pk_mul_f32 v[36:37], v[40:41], v[38:39] op_sel_hi:[0,1]
	v_pk_mul_f32 v[12:13], v[12:13], v[36:37]
	global_load_dwordx4 v[36:39], v41, s[8:9] offset:224
	s_waitcnt vmcnt(0)
	v_pk_mul_f32 v[36:37], v[40:41], v[36:37] op_sel_hi:[0,1]
	v_pk_mul_f32 v[14:15], v[14:15], v[36:37]
	v_pk_mul_f32 v[36:37], v[40:41], v[38:39] op_sel_hi:[0,1]
	v_pk_mul_f32 v[16:17], v[16:17], v[36:37]
	global_load_dwordx4 v[36:39], v41, s[8:9]
	s_waitcnt vmcnt(0)
	v_pk_mul_f32 v[36:37], v[40:41], v[36:37] op_sel_hi:[0,1]
	v_pk_mul_f32 v[24:25], v[24:25], v[36:37]
	v_pk_mul_f32 v[36:37], v[40:41], v[38:39] op_sel_hi:[0,1]
	v_pk_mul_f32 v[26:27], v[26:27], v[36:37]
	global_load_dwordx4 v[36:39], v41, s[8:9] offset:32
	v_cvt_pk_bf16_f32 v24, v24, v25
	v_cvt_pk_bf16_f32 v25, v26, v27
	s_waitcnt vmcnt(0)
	v_pk_mul_f32 v[36:37], v[40:41], v[36:37] op_sel_hi:[0,1]
	v_pk_mul_f32 v[28:29], v[28:29], v[36:37]
	v_pk_mul_f32 v[36:37], v[40:41], v[38:39] op_sel_hi:[0,1]
	v_pk_mul_f32 v[30:31], v[30:31], v[36:37]
	global_load_dwordx4 v[36:39], v41, s[8:9] offset:64
	s_waitcnt vmcnt(0)
	v_pk_mul_f32 v[36:37], v[40:41], v[36:37] op_sel_hi:[0,1]
	v_pk_mul_f32 v[32:33], v[32:33], v[36:37]
	v_pk_mul_f32 v[36:37], v[40:41], v[38:39] op_sel_hi:[0,1]
	v_pk_mul_f32 v[34:35], v[34:35], v[36:37]
	global_load_dwordx4 v[36:39], v41, s[8:9] offset:96
	s_nop 0
	global_store_dwordx2 v[18:19], v[24:25], off offset:1024
	global_store_dwordx2 v[18:19], v[2:3], off offset:1088
	v_cvt_pk_bf16_f32 v2, v28, v29
	v_cvt_pk_bf16_f32 v3, v30, v31
	global_store_dwordx2 v[18:19], v[2:3], off offset:1040
	global_store_dwordx2 v[18:19], v[4:5], off offset:1104
	v_cvt_pk_bf16_f32 v2, v32, v33
	v_cvt_pk_bf16_f32 v3, v34, v35
	v_cvt_pk_bf16_f32 v4, v10, v11
	v_cvt_pk_bf16_f32 v5, v12, v13
	global_store_dwordx2 v[18:19], v[2:3], off offset:1056
	global_store_dwordx2 v[18:19], v[4:5], off offset:1120
	v_cvt_pk_bf16_f32 v4, v14, v15
	v_cvt_pk_bf16_f32 v5, v16, v17
	s_waitcnt vmcnt(6)
	v_pk_mul_f32 v[36:37], v[40:41], v[36:37] op_sel_hi:[0,1]
	v_pk_mul_f32 v[20:21], v[20:21], v[36:37]
	v_pk_mul_f32 v[36:37], v[40:41], v[38:39] op_sel_hi:[0,1]
	v_pk_mul_f32 v[22:23], v[22:23], v[36:37]
	v_cvt_pk_bf16_f32 v2, v20, v21
	v_cvt_pk_bf16_f32 v3, v22, v23
	global_store_dwordx2 v[18:19], v[2:3], off offset:1072
	global_store_dwordx2 v[18:19], v[4:5], off offset:1136
	s_branch .LBB0_951
